# hg_b: all 132 operand loads of the 66 units issued before a single wait, then the 66-step state chain with stores (was 6 exposed load batches)
# baseline (speedup 1.0000x reference)
; __device__ __forceinline__ void ph_hg_b(const Frame& F) {
;     const float* SLOC = (const float*)(F.R1 + R1_SLOC); const float* DL = (const float*)(F.R1 + R1_DL); float* SST = (float*)(F.R1 + R1_SST);
;     for (int idx = F.wg * 512 + F.tid; idx < 64 * 4096; idx += F.G * 512) {
;         const int seq = idx >> 12, e = idx & 4095, ln = e & 63, reg = e >> 6, i = reg & 3, kt = reg >> 4, k = 16 * kt + 4 * (ln >> 4) + i;
;         float s = 0.f;
;         for (int u0 = 0; u0 < HG_NU; u0 += 11) {
;             float sl[11], dl[11];
; #pragma unroll
;             for (int q = 0; q < 11; ++q) { sl[q] = SLOC[((size_t)seq * HG_NU + u0 + q) * 4096 + e]; dl[q] = DL[((size_t)seq * HG_NU + u0 + q) * 64 + k]; }
;             asm volatile("" ::: "memory"); __builtin_amdgcn_sched_barrier(0);
; #pragma unroll
;             for (int q = 0; q < 11; ++q) { SST[((size_t)seq * HG_NU + u0 + q) * 4096 + e] = s; s = dl[q] * s + sl[q]; }
;         }
;     }
.LBB0_831:
	v_lshl_add_u64 v[6:7], s[62:63], 0, v[4:5]
	v_add_co_u32_e32 v10, vcc, 0x2fcd8000, v6
	s_nop 1
	v_addc_co_u32_e32 v11, vcc, 0, v7, vcc
	v_lshl_add_u64 v[12:13], s[62:63], 0, v[0:1]
	v_add_co_u32_e32 v12, vcc, 0x380d8000, v12
	s_nop 1
	v_addc_co_u32_e32 v13, vcc, 0, v13, vcc
	s_mov_b64 s[6:7], 0x4000
	global_load_dword v34, v[10:11], off
	v_lshl_add_u64 v[10:11], v[10:11], 0, s[6:7]
	global_load_dword v100, v[12:13], off
	global_load_dword v35, v[10:11], off
	v_lshl_add_u64 v[10:11], v[10:11], 0, s[6:7]
	global_load_dword v101, v[12:13], off offset:256
	global_load_dword v36, v[10:11], off
	v_lshl_add_u64 v[10:11], v[10:11], 0, s[6:7]
	global_load_dword v102, v[12:13], off offset:512
	global_load_dword v37, v[10:11], off
	v_lshl_add_u64 v[10:11], v[10:11], 0, s[6:7]
	global_load_dword v103, v[12:13], off offset:768
	global_load_dword v38, v[10:11], off
	v_lshl_add_u64 v[10:11], v[10:11], 0, s[6:7]
	global_load_dword v104, v[12:13], off offset:1024
	global_load_dword v39, v[10:11], off
	v_lshl_add_u64 v[10:11], v[10:11], 0, s[6:7]
	global_load_dword v105, v[12:13], off offset:1280
	global_load_dword v40, v[10:11], off
	v_lshl_add_u64 v[10:11], v[10:11], 0, s[6:7]
	global_load_dword v106, v[12:13], off offset:1536
	global_load_dword v41, v[10:11], off
	v_lshl_add_u64 v[10:11], v[10:11], 0, s[6:7]
	global_load_dword v107, v[12:13], off offset:1792
	global_load_dword v42, v[10:11], off
	v_lshl_add_u64 v[10:11], v[10:11], 0, s[6:7]
	global_load_dword v108, v[12:13], off offset:2048
	global_load_dword v43, v[10:11], off
	v_lshl_add_u64 v[10:11], v[10:11], 0, s[6:7]
	global_load_dword v109, v[12:13], off offset:2304
	global_load_dword v44, v[10:11], off
	v_lshl_add_u64 v[10:11], v[10:11], 0, s[6:7]
	global_load_dword v110, v[12:13], off offset:2560
	global_load_dword v45, v[10:11], off
	v_lshl_add_u64 v[10:11], v[10:11], 0, s[6:7]
	global_load_dword v111, v[12:13], off offset:2816
	global_load_dword v46, v[10:11], off
	v_lshl_add_u64 v[10:11], v[10:11], 0, s[6:7]
	global_load_dword v112, v[12:13], off offset:3072
	global_load_dword v47, v[10:11], off
	v_lshl_add_u64 v[10:11], v[10:11], 0, s[6:7]
	global_load_dword v113, v[12:13], off offset:3328
	global_load_dword v48, v[10:11], off
	v_lshl_add_u64 v[10:11], v[10:11], 0, s[6:7]
	global_load_dword v114, v[12:13], off offset:3584
	global_load_dword v49, v[10:11], off
	v_lshl_add_u64 v[10:11], v[10:11], 0, s[6:7]
	global_load_dword v115, v[12:13], off offset:3840
	v_add_co_u32_e32 v12, vcc, 0x1000, v12
	s_nop 1
	v_addc_co_u32_e32 v13, vcc, 0, v13, vcc
	global_load_dword v50, v[10:11], off
	v_lshl_add_u64 v[10:11], v[10:11], 0, s[6:7]
	global_load_dword v116, v[12:13], off
	global_load_dword v51, v[10:11], off
	v_lshl_add_u64 v[10:11], v[10:11], 0, s[6:7]
	global_load_dword v117, v[12:13], off offset:256
	global_load_dword v52, v[10:11], off
	v_lshl_add_u64 v[10:11], v[10:11], 0, s[6:7]
	global_load_dword v118, v[12:13], off offset:512
	global_load_dword v53, v[10:11], off
	v_lshl_add_u64 v[10:11], v[10:11], 0, s[6:7]
	global_load_dword v119, v[12:13], off offset:768
	global_load_dword v54, v[10:11], off
	v_lshl_add_u64 v[10:11], v[10:11], 0, s[6:7]
	global_load_dword v120, v[12:13], off offset:1024
	global_load_dword v55, v[10:11], off
	v_lshl_add_u64 v[10:11], v[10:11], 0, s[6:7]
	global_load_dword v121, v[12:13], off offset:1280
	global_load_dword v56, v[10:11], off
	v_lshl_add_u64 v[10:11], v[10:11], 0, s[6:7]
	global_load_dword v122, v[12:13], off offset:1536
	global_load_dword v57, v[10:11], off
	v_lshl_add_u64 v[10:11], v[10:11], 0, s[6:7]
	global_load_dword v123, v[12:13], off offset:1792
	global_load_dword v58, v[10:11], off
	v_lshl_add_u64 v[10:11], v[10:11], 0, s[6:7]
	global_load_dword v124, v[12:13], off offset:2048
	global_load_dword v59, v[10:11], off
	v_lshl_add_u64 v[10:11], v[10:11], 0, s[6:7]
	global_load_dword v125, v[12:13], off offset:2304
	global_load_dword v60, v[10:11], off
	v_lshl_add_u64 v[10:11], v[10:11], 0, s[6:7]
	global_load_dword v126, v[12:13], off offset:2560
	global_load_dword v61, v[10:11], off
	v_lshl_add_u64 v[10:11], v[10:11], 0, s[6:7]
	global_load_dword v127, v[12:13], off offset:2816
	global_load_dword v62, v[10:11], off
	v_lshl_add_u64 v[10:11], v[10:11], 0, s[6:7]
	global_load_dword v128, v[12:13], off offset:3072
	global_load_dword v63, v[10:11], off
	v_lshl_add_u64 v[10:11], v[10:11], 0, s[6:7]
	global_load_dword v129, v[12:13], off offset:3328
	global_load_dword v64, v[10:11], off
	v_lshl_add_u64 v[10:11], v[10:11], 0, s[6:7]
	global_load_dword v130, v[12:13], off offset:3584
	global_load_dword v65, v[10:11], off
	v_lshl_add_u64 v[10:11], v[10:11], 0, s[6:7]
	global_load_dword v131, v[12:13], off offset:3840
	v_add_co_u32_e32 v12, vcc, 0x1000, v12
	s_nop 1
	v_addc_co_u32_e32 v13, vcc, 0, v13, vcc
	global_load_dword v66, v[10:11], off
	v_lshl_add_u64 v[10:11], v[10:11], 0, s[6:7]
	global_load_dword v132, v[12:13], off
	global_load_dword v67, v[10:11], off
	v_lshl_add_u64 v[10:11], v[10:11], 0, s[6:7]
	global_load_dword v133, v[12:13], off offset:256
	global_load_dword v68, v[10:11], off
	v_lshl_add_u64 v[10:11], v[10:11], 0, s[6:7]
	global_load_dword v134, v[12:13], off offset:512
	global_load_dword v69, v[10:11], off
	v_lshl_add_u64 v[10:11], v[10:11], 0, s[6:7]
	global_load_dword v135, v[12:13], off offset:768
	global_load_dword v70, v[10:11], off
	v_lshl_add_u64 v[10:11], v[10:11], 0, s[6:7]
	global_load_dword v136, v[12:13], off offset:1024
	global_load_dword v71, v[10:11], off
	v_lshl_add_u64 v[10:11], v[10:11], 0, s[6:7]
	global_load_dword v137, v[12:13], off offset:1280
	global_load_dword v72, v[10:11], off
	v_lshl_add_u64 v[10:11], v[10:11], 0, s[6:7]
; __device__ __forceinline__ void ph_hg_b(const Frame& F) {
;     const float* SLOC = (const float*)(F.R1 + R1_SLOC); const float* DL = (const float*)(F.R1 + R1_DL); float* SST = (float*)(F.R1 + R1_SST);
;     for (int idx = F.wg * 512 + F.tid; idx < 64 * 4096; idx += F.G * 512) {
;         const int seq = idx >> 12, e = idx & 4095, ln = e & 63, reg = e >> 6, i = reg & 3, kt = reg >> 4, k = 16 * kt + 4 * (ln >> 4) + i;
;         float s = 0.f;
;         for (int u0 = 0; u0 < HG_NU; u0 += 11) {
;             float sl[11], dl[11];
; #pragma unroll
;             for (int q = 0; q < 11; ++q) { sl[q] = SLOC[((size_t)seq * HG_NU + u0 + q) * 4096 + e]; dl[q] = DL[((size_t)seq * HG_NU + u0 + q) * 64 + k]; }
;             asm volatile("" ::: "memory"); __builtin_amdgcn_sched_barrier(0);
; #pragma unroll
;             for (int q = 0; q < 11; ++q) { SST[((size_t)seq * HG_NU + u0 + q) * 4096 + e] = s; s = dl[q] * s + sl[q]; }
;         }
;     }
	global_load_dword v138, v[12:13], off offset:1536
	global_load_dword v73, v[10:11], off
	v_lshl_add_u64 v[10:11], v[10:11], 0, s[6:7]
	global_load_dword v139, v[12:13], off offset:1792
	global_load_dword v74, v[10:11], off
	v_lshl_add_u64 v[10:11], v[10:11], 0, s[6:7]
	global_load_dword v140, v[12:13], off offset:2048
	global_load_dword v75, v[10:11], off
	v_lshl_add_u64 v[10:11], v[10:11], 0, s[6:7]
	global_load_dword v141, v[12:13], off offset:2304
	global_load_dword v76, v[10:11], off
	v_lshl_add_u64 v[10:11], v[10:11], 0, s[6:7]
	global_load_dword v142, v[12:13], off offset:2560
	global_load_dword v77, v[10:11], off
	v_lshl_add_u64 v[10:11], v[10:11], 0, s[6:7]
	global_load_dword v143, v[12:13], off offset:2816
	global_load_dword v78, v[10:11], off
	v_lshl_add_u64 v[10:11], v[10:11], 0, s[6:7]
	global_load_dword v145, v[12:13], off offset:3072
	global_load_dword v79, v[10:11], off
	v_lshl_add_u64 v[10:11], v[10:11], 0, s[6:7]
	global_load_dword v146, v[12:13], off offset:3328
	global_load_dword v80, v[10:11], off
	v_lshl_add_u64 v[10:11], v[10:11], 0, s[6:7]
	global_load_dword v147, v[12:13], off offset:3584
	global_load_dword v81, v[10:11], off
	v_lshl_add_u64 v[10:11], v[10:11], 0, s[6:7]
	global_load_dword v148, v[12:13], off offset:3840
	v_add_co_u32_e32 v12, vcc, 0x1000, v12
	s_nop 1
	v_addc_co_u32_e32 v13, vcc, 0, v13, vcc
	global_load_dword v82, v[10:11], off
	v_lshl_add_u64 v[10:11], v[10:11], 0, s[6:7]
	global_load_dword v149, v[12:13], off
	global_load_dword v83, v[10:11], off
	v_lshl_add_u64 v[10:11], v[10:11], 0, s[6:7]
	global_load_dword v150, v[12:13], off offset:256
	global_load_dword v84, v[10:11], off
	v_lshl_add_u64 v[10:11], v[10:11], 0, s[6:7]
	global_load_dword v151, v[12:13], off offset:512
	global_load_dword v85, v[10:11], off
	v_lshl_add_u64 v[10:11], v[10:11], 0, s[6:7]
	global_load_dword v152, v[12:13], off offset:768
	global_load_dword v86, v[10:11], off
	v_lshl_add_u64 v[10:11], v[10:11], 0, s[6:7]
	global_load_dword v153, v[12:13], off offset:1024
	global_load_dword v87, v[10:11], off
	v_lshl_add_u64 v[10:11], v[10:11], 0, s[6:7]
	global_load_dword v154, v[12:13], off offset:1280
	global_load_dword v88, v[10:11], off
	v_lshl_add_u64 v[10:11], v[10:11], 0, s[6:7]
	global_load_dword v155, v[12:13], off offset:1536
	global_load_dword v89, v[10:11], off
	v_lshl_add_u64 v[10:11], v[10:11], 0, s[6:7]
	global_load_dword v156, v[12:13], off offset:1792
	global_load_dword v90, v[10:11], off
	v_lshl_add_u64 v[10:11], v[10:11], 0, s[6:7]
	global_load_dword v157, v[12:13], off offset:2048
	global_load_dword v91, v[10:11], off
	v_lshl_add_u64 v[10:11], v[10:11], 0, s[6:7]
	global_load_dword v158, v[12:13], off offset:2304
	global_load_dword v92, v[10:11], off
	v_lshl_add_u64 v[10:11], v[10:11], 0, s[6:7]
	global_load_dword v159, v[12:13], off offset:2560
	global_load_dword v93, v[10:11], off
	v_lshl_add_u64 v[10:11], v[10:11], 0, s[6:7]
	global_load_dword v160, v[12:13], off offset:2816
	global_load_dword v94, v[10:11], off
	v_lshl_add_u64 v[10:11], v[10:11], 0, s[6:7]
	global_load_dword v161, v[12:13], off offset:3072
	global_load_dword v95, v[10:11], off
	v_lshl_add_u64 v[10:11], v[10:11], 0, s[6:7]
	global_load_dword v162, v[12:13], off offset:3328
	global_load_dword v96, v[10:11], off
	v_lshl_add_u64 v[10:11], v[10:11], 0, s[6:7]
	global_load_dword v163, v[12:13], off offset:3584
	global_load_dword v97, v[10:11], off
	v_lshl_add_u64 v[10:11], v[10:11], 0, s[6:7]
	global_load_dword v164, v[12:13], off offset:3840
	v_add_co_u32_e32 v12, vcc, 0x1000, v12
	s_nop 1
	v_addc_co_u32_e32 v13, vcc, 0, v13, vcc
	global_load_dword v98, v[10:11], off
	v_lshl_add_u64 v[10:11], v[10:11], 0, s[6:7]
	global_load_dword v165, v[12:13], off
	global_load_dword v99, v[10:11], off
	global_load_dword v166, v[12:13], off offset:256
	v_add_co_u32_e32 v10, vcc, 0x33ed8000, v6
	s_nop 1
	v_addc_co_u32_e32 v11, vcc, 0, v7, vcc
	s_waitcnt vmcnt(0)
	global_store_dword v[10:11], v9, off
	v_fmac_f32_e32 v34, v9, v100
	v_lshl_add_u64 v[10:11], v[10:11], 0, s[6:7]
	global_store_dword v[10:11], v34, off
	v_fmac_f32_e32 v35, v34, v101
	v_lshl_add_u64 v[10:11], v[10:11], 0, s[6:7]
	global_store_dword v[10:11], v35, off
	v_fmac_f32_e32 v36, v35, v102
	v_lshl_add_u64 v[10:11], v[10:11], 0, s[6:7]
	global_store_dword v[10:11], v36, off
	v_fmac_f32_e32 v37, v36, v103
	v_lshl_add_u64 v[10:11], v[10:11], 0, s[6:7]
	global_store_dword v[10:11], v37, off
	v_fmac_f32_e32 v38, v37, v104
	v_lshl_add_u64 v[10:11], v[10:11], 0, s[6:7]
	global_store_dword v[10:11], v38, off
	v_fmac_f32_e32 v39, v38, v105
	v_lshl_add_u64 v[10:11], v[10:11], 0, s[6:7]
	global_store_dword v[10:11], v39, off
	v_fmac_f32_e32 v40, v39, v106
	v_lshl_add_u64 v[10:11], v[10:11], 0, s[6:7]
	global_store_dword v[10:11], v40, off
	v_fmac_f32_e32 v41, v40, v107
	v_lshl_add_u64 v[10:11], v[10:11], 0, s[6:7]
	global_store_dword v[10:11], v41, off
	v_fmac_f32_e32 v42, v41, v108
	v_lshl_add_u64 v[10:11], v[10:11], 0, s[6:7]
	global_store_dword v[10:11], v42, off
	v_fmac_f32_e32 v43, v42, v109
	v_lshl_add_u64 v[10:11], v[10:11], 0, s[6:7]
	global_store_dword v[10:11], v43, off
	v_fmac_f32_e32 v44, v43, v110
	v_lshl_add_u64 v[10:11], v[10:11], 0, s[6:7]
	global_store_dword v[10:11], v44, off
	v_fmac_f32_e32 v45, v44, v111
	v_lshl_add_u64 v[10:11], v[10:11], 0, s[6:7]
	global_store_dword v[10:11], v45, off
	v_fmac_f32_e32 v46, v45, v112
	v_lshl_add_u64 v[10:11], v[10:11], 0, s[6:7]
	global_store_dword v[10:11], v46, off
	v_fmac_f32_e32 v47, v46, v113
	v_lshl_add_u64 v[10:11], v[10:11], 0, s[6:7]
	global_store_dword v[10:11], v47, off
	v_fmac_f32_e32 v48, v47, v114
	v_lshl_add_u64 v[10:11], v[10:11], 0, s[6:7]
; __device__ __forceinline__ void ph_hg_b(const Frame& F) {
;     const float* SLOC = (const float*)(F.R1 + R1_SLOC); const float* DL = (const float*)(F.R1 + R1_DL); float* SST = (float*)(F.R1 + R1_SST);
;     for (int idx = F.wg * 512 + F.tid; idx < 64 * 4096; idx += F.G * 512) {
;         const int seq = idx >> 12, e = idx & 4095, ln = e & 63, reg = e >> 6, i = reg & 3, kt = reg >> 4, k = 16 * kt + 4 * (ln >> 4) + i;
;         float s = 0.f;
;         for (int u0 = 0; u0 < HG_NU; u0 += 11) {
;             float sl[11], dl[11];
; #pragma unroll
;             for (int q = 0; q < 11; ++q) { sl[q] = SLOC[((size_t)seq * HG_NU + u0 + q) * 4096 + e]; dl[q] = DL[((size_t)seq * HG_NU + u0 + q) * 64 + k]; }
;             asm volatile("" ::: "memory"); __builtin_amdgcn_sched_barrier(0);
; #pragma unroll
;             for (int q = 0; q < 11; ++q) { SST[((size_t)seq * HG_NU + u0 + q) * 4096 + e] = s; s = dl[q] * s + sl[q]; }
;         }
;     }
	global_store_dword v[10:11], v48, off
	v_fmac_f32_e32 v49, v48, v115
	v_lshl_add_u64 v[10:11], v[10:11], 0, s[6:7]
	global_store_dword v[10:11], v49, off
	v_fmac_f32_e32 v50, v49, v116
	v_lshl_add_u64 v[10:11], v[10:11], 0, s[6:7]
	global_store_dword v[10:11], v50, off
	v_fmac_f32_e32 v51, v50, v117
	v_lshl_add_u64 v[10:11], v[10:11], 0, s[6:7]
	global_store_dword v[10:11], v51, off
	v_fmac_f32_e32 v52, v51, v118
	v_lshl_add_u64 v[10:11], v[10:11], 0, s[6:7]
	global_store_dword v[10:11], v52, off
	v_fmac_f32_e32 v53, v52, v119
	v_lshl_add_u64 v[10:11], v[10:11], 0, s[6:7]
	global_store_dword v[10:11], v53, off
	v_fmac_f32_e32 v54, v53, v120
	v_lshl_add_u64 v[10:11], v[10:11], 0, s[6:7]
	global_store_dword v[10:11], v54, off
	v_fmac_f32_e32 v55, v54, v121
	v_lshl_add_u64 v[10:11], v[10:11], 0, s[6:7]
	global_store_dword v[10:11], v55, off
	v_fmac_f32_e32 v56, v55, v122
	v_lshl_add_u64 v[10:11], v[10:11], 0, s[6:7]
	global_store_dword v[10:11], v56, off
	v_fmac_f32_e32 v57, v56, v123
	v_lshl_add_u64 v[10:11], v[10:11], 0, s[6:7]
	global_store_dword v[10:11], v57, off
	v_fmac_f32_e32 v58, v57, v124
	v_lshl_add_u64 v[10:11], v[10:11], 0, s[6:7]
	global_store_dword v[10:11], v58, off
	v_fmac_f32_e32 v59, v58, v125
	v_lshl_add_u64 v[10:11], v[10:11], 0, s[6:7]
	global_store_dword v[10:11], v59, off
	v_fmac_f32_e32 v60, v59, v126
	v_lshl_add_u64 v[10:11], v[10:11], 0, s[6:7]
	global_store_dword v[10:11], v60, off
	v_fmac_f32_e32 v61, v60, v127
	v_lshl_add_u64 v[10:11], v[10:11], 0, s[6:7]
	global_store_dword v[10:11], v61, off
	v_fmac_f32_e32 v62, v61, v128
	v_lshl_add_u64 v[10:11], v[10:11], 0, s[6:7]
	global_store_dword v[10:11], v62, off
	v_fmac_f32_e32 v63, v62, v129
	v_lshl_add_u64 v[10:11], v[10:11], 0, s[6:7]
	global_store_dword v[10:11], v63, off
	v_fmac_f32_e32 v64, v63, v130
	v_lshl_add_u64 v[10:11], v[10:11], 0, s[6:7]
	global_store_dword v[10:11], v64, off
	v_fmac_f32_e32 v65, v64, v131
	v_lshl_add_u64 v[10:11], v[10:11], 0, s[6:7]
	global_store_dword v[10:11], v65, off
	v_fmac_f32_e32 v66, v65, v132
	v_lshl_add_u64 v[10:11], v[10:11], 0, s[6:7]
	global_store_dword v[10:11], v66, off
	v_fmac_f32_e32 v67, v66, v133
	v_lshl_add_u64 v[10:11], v[10:11], 0, s[6:7]
	global_store_dword v[10:11], v67, off
	v_fmac_f32_e32 v68, v67, v134
	v_lshl_add_u64 v[10:11], v[10:11], 0, s[6:7]
	global_store_dword v[10:11], v68, off
	v_fmac_f32_e32 v69, v68, v135
	v_lshl_add_u64 v[10:11], v[10:11], 0, s[6:7]
	global_store_dword v[10:11], v69, off
	v_fmac_f32_e32 v70, v69, v136
	v_lshl_add_u64 v[10:11], v[10:11], 0, s[6:7]
	global_store_dword v[10:11], v70, off
	v_fmac_f32_e32 v71, v70, v137
	v_lshl_add_u64 v[10:11], v[10:11], 0, s[6:7]
	global_store_dword v[10:11], v71, off
	v_fmac_f32_e32 v72, v71, v138
	v_lshl_add_u64 v[10:11], v[10:11], 0, s[6:7]
	global_store_dword v[10:11], v72, off
	v_fmac_f32_e32 v73, v72, v139
	v_lshl_add_u64 v[10:11], v[10:11], 0, s[6:7]
	global_store_dword v[10:11], v73, off
	v_fmac_f32_e32 v74, v73, v140
	v_lshl_add_u64 v[10:11], v[10:11], 0, s[6:7]
	global_store_dword v[10:11], v74, off
	v_fmac_f32_e32 v75, v74, v141
	v_lshl_add_u64 v[10:11], v[10:11], 0, s[6:7]
	global_store_dword v[10:11], v75, off
	v_fmac_f32_e32 v76, v75, v142
	v_lshl_add_u64 v[10:11], v[10:11], 0, s[6:7]
	global_store_dword v[10:11], v76, off
	v_fmac_f32_e32 v77, v76, v143
	v_lshl_add_u64 v[10:11], v[10:11], 0, s[6:7]
	global_store_dword v[10:11], v77, off
	v_fmac_f32_e32 v78, v77, v145
	v_lshl_add_u64 v[10:11], v[10:11], 0, s[6:7]
	global_store_dword v[10:11], v78, off
	v_fmac_f32_e32 v79, v78, v146
	v_lshl_add_u64 v[10:11], v[10:11], 0, s[6:7]
	global_store_dword v[10:11], v79, off
	v_fmac_f32_e32 v80, v79, v147
	v_lshl_add_u64 v[10:11], v[10:11], 0, s[6:7]
	global_store_dword v[10:11], v80, off
	v_fmac_f32_e32 v81, v80, v148
	v_lshl_add_u64 v[10:11], v[10:11], 0, s[6:7]
	global_store_dword v[10:11], v81, off
	v_fmac_f32_e32 v82, v81, v149
	v_lshl_add_u64 v[10:11], v[10:11], 0, s[6:7]
	global_store_dword v[10:11], v82, off
	v_fmac_f32_e32 v83, v82, v150
	v_lshl_add_u64 v[10:11], v[10:11], 0, s[6:7]
	global_store_dword v[10:11], v83, off
	v_fmac_f32_e32 v84, v83, v151
	v_lshl_add_u64 v[10:11], v[10:11], 0, s[6:7]
	global_store_dword v[10:11], v84, off
	v_fmac_f32_e32 v85, v84, v152
	v_lshl_add_u64 v[10:11], v[10:11], 0, s[6:7]
	global_store_dword v[10:11], v85, off
	v_fmac_f32_e32 v86, v85, v153
	v_lshl_add_u64 v[10:11], v[10:11], 0, s[6:7]
	global_store_dword v[10:11], v86, off
	v_fmac_f32_e32 v87, v86, v154
	v_lshl_add_u64 v[10:11], v[10:11], 0, s[6:7]
	global_store_dword v[10:11], v87, off
	v_fmac_f32_e32 v88, v87, v155
	v_lshl_add_u64 v[10:11], v[10:11], 0, s[6:7]
	global_store_dword v[10:11], v88, off
	v_fmac_f32_e32 v89, v88, v156
	v_lshl_add_u64 v[10:11], v[10:11], 0, s[6:7]
	global_store_dword v[10:11], v89, off
	v_fmac_f32_e32 v90, v89, v157
	v_lshl_add_u64 v[10:11], v[10:11], 0, s[6:7]
	global_store_dword v[10:11], v90, off
	v_fmac_f32_e32 v91, v90, v158
	v_lshl_add_u64 v[10:11], v[10:11], 0, s[6:7]
	global_store_dword v[10:11], v91, off
	v_fmac_f32_e32 v92, v91, v159
	v_lshl_add_u64 v[10:11], v[10:11], 0, s[6:7]
	global_store_dword v[10:11], v92, off
	v_fmac_f32_e32 v93, v92, v160
	v_lshl_add_u64 v[10:11], v[10:11], 0, s[6:7]
	global_store_dword v[10:11], v93, off
	v_fmac_f32_e32 v94, v93, v161
	v_lshl_add_u64 v[10:11], v[10:11], 0, s[6:7]
	global_store_dword v[10:11], v94, off
	v_fmac_f32_e32 v95, v94, v162
	v_lshl_add_u64 v[10:11], v[10:11], 0, s[6:7]
	global_store_dword v[10:11], v95, off
	v_fmac_f32_e32 v96, v95, v163
	v_lshl_add_u64 v[10:11], v[10:11], 0, s[6:7]
	global_store_dword v[10:11], v96, off
	v_fmac_f32_e32 v97, v96, v164
	v_lshl_add_u64 v[10:11], v[10:11], 0, s[6:7]
	global_store_dword v[10:11], v97, off
	v_fmac_f32_e32 v98, v97, v165
	v_lshl_add_u64 v[10:11], v[10:11], 0, s[6:7]
	global_store_dword v[10:11], v98, off
	v_fmac_f32_e32 v99, v98, v166
	v_readlane_b32 s6, v251, 53
	s_mov_b32 s2, 0x3ffff
	s_nop 0
	v_add_u32_e32 v3, s6, v3
	v_cmp_lt_i32_e32 vcc, s2, v3
	s_or_b64 s[4:5], vcc, s[4:5]
	v_add_u16_e32 v8, s6, v8
	s_andn2_b64 exec, exec, s[4:5]
	s_cbranch_execnz .LBB0_830
